# speedup vs baseline: 1.0036x; 1.0036x over previous
.LBB2_1:
	s_add_i32 s13, s3, -4
	s_and_b32 s13, s13, 4
	s_mulk_i32 s13, 0x2400
	v_add_u32_e32 v124, s13, v120
	ds_read_b128 v[96:99], v124
	ds_read_b128 v[126:129], v124 offset:32
	ds_read_b128 v[130:133], v124 offset:4608
	ds_read_b128 v[134:137], v124 offset:4640
	v_lshl_add_u64 v[118:119], v[108:109], 0, s[4:5]
	v_add_co_u32_e32 v150, vcc, s12, v118
	s_waitcnt vmcnt(7) lgkmcnt(3)
	v_mfma_f32_32x32x16_f16 v[48:63], v[96:99], v[88:91], 0
	v_mov_b32_e32 v125, v116
	v_lshl_add_u64 v[116:117], v[110:111], 0, s[4:5]
	v_addc_co_u32_e32 v151, vcc, 0, v119, vcc
	v_mov_b32_e32 v123, v100
	v_lshl_add_u64 v[102:103], v[112:113], 0, s[6:7]
	v_lshl_add_u64 v[100:101], v[114:115], 0, s[6:7]
	s_waitcnt lgkmcnt(1)
	v_mfma_f32_32x32x16_f16 v[32:47], v[130:133], v[88:91], 0
	v_add_co_u32_e32 v158, vcc, s12, v116
	s_and_b32 s13, s3, 4
	s_nop 0
	v_addc_co_u32_e32 v159, vcc, 0, v117, vcc
	global_load_dwordx4 v[220:223], v[102:103], off offset:128
	global_load_dwordx4 v[224:227], v[100:101], off offset:128
	v_add_co_u32_e32 v102, vcc, s1, v102
	s_nop 1
	v_addc_co_u32_e32 v103, vcc, 0, v103, vcc
	v_add_co_u32_e32 v100, vcc, s1, v100
	s_nop 1
	v_addc_co_u32_e32 v101, vcc, 0, v101, vcc
	global_load_dwordx4 v[228:231], v[150:151], off offset:-4096
	global_load_dwordx4 v[232:235], v[150:151], off
	global_load_dwordx4 v[236:239], v[158:159], off offset:-4096
	global_load_dwordx4 v[240:243], v[158:159], off
	global_load_dwordx4 v[244:247], v[102:103], off offset:128
	global_load_dwordx4 v[248:251], v[100:101], off offset:128
	s_mulk_i32 s13, 0x2400
	v_add_u32_e32 v218, s13, v121
	s_waitcnt vmcnt(13)
	v_mfma_f32_32x32x16_f16 v[48:63], v[96:99], v[92:95], v[48:63]
	s_add_u32 s6, s6, 0x80
	s_addc_u32 s7, s7, 0
	s_add_i32 s3, s3, 4
	s_add_u32 s4, s4, 0x2000
	s_addc_u32 s5, s5, 0
	s_cmpk_eq_i32 s6, 0x780
	v_mfma_f32_32x32x16_f16 v[32:47], v[130:133], v[92:95], v[32:47]
	ds_read_b128 v[96:99], v124 offset:9216
	ds_read_b128 v[130:133], v124 offset:9248
	s_waitcnt lgkmcnt(1)
	v_mfma_f32_32x32x16_f16 v[48:63], v[96:99], v[88:91], v[48:63]
	ds_read_b128 v[138:141], v124 offset:13824
	ds_read_b128 v[96:99], v124 offset:13856
	s_waitcnt lgkmcnt(1)
	v_mfma_f32_32x32x16_f16 v[32:47], v[138:141], v[88:91], v[32:47]
	v_mfma_f32_32x32x16_f16 v[48:63], v[126:129], v[80:83], v[48:63]
	v_mfma_f32_32x32x16_f16 v[32:47], v[134:137], v[80:83], v[32:47]
	s_waitcnt vmcnt(12)
	v_mfma_f32_32x32x16_f16 v[48:63], v[126:129], v[84:87], v[48:63]
	v_mfma_f32_32x32x16_f16 v[32:47], v[134:137], v[84:87], v[32:47]
	v_mfma_f32_32x32x16_f16 v[48:63], v[130:133], v[80:83], v[48:63]
	s_waitcnt lgkmcnt(0)
	v_mfma_f32_32x32x16_f16 v[32:47], v[96:99], v[80:83], v[32:47]
	ds_read_b128 v[96:99], v124 offset:64
	ds_read_b128 v[126:129], v124 offset:96
	ds_read_b128 v[130:133], v124 offset:4672
	ds_read_b128 v[134:137], v124 offset:4704
	s_waitcnt vmcnt(11) lgkmcnt(3)
	v_mfma_f32_32x32x16_f16 v[48:63], v[96:99], v[72:75], v[48:63]
	s_waitcnt lgkmcnt(1)
	v_mfma_f32_32x32x16_f16 v[32:47], v[130:133], v[72:75], v[32:47]
	s_waitcnt vmcnt(9)
	v_mfma_f32_32x32x16_f16 v[48:63], v[96:99], v[76:79], v[48:63]
	v_mfma_f32_32x32x16_f16 v[32:47], v[130:133], v[76:79], v[32:47]
	ds_read_b128 v[96:99], v124 offset:9280
	ds_read_b128 v[130:133], v124 offset:9312
	s_waitcnt lgkmcnt(1)
	v_mfma_f32_32x32x16_f16 v[48:63], v[96:99], v[72:75], v[48:63]
	ds_read_b128 v[96:99], v124 offset:13888
	ds_read_b128 v[142:145], v124 offset:13920
	ds_read_b128 v[170:173], v124 offset:23040
	ds_read_b128 v[174:177], v124 offset:18432
	ds_read_b128 v[178:181], v124 offset:18464
	ds_read_b128 v[182:185], v124 offset:27648
	ds_read_b128 v[186:189], v124 offset:27680
	v_mfma_f32_32x32x16_f16 v[48:63], v[126:129], v[64:67], v[48:63]
	s_waitcnt lgkmcnt(6)
	v_mfma_f32_32x32x16_f16 v[32:47], v[96:99], v[72:75], v[32:47]
	s_waitcnt vmcnt(8)
	v_mfma_f32_32x32x16_f16 v[48:63], v[126:129], v[68:71], v[48:63]
	ds_read_b128 v[126:129], v124 offset:23072
	ds_read_b128 v[190:193], v124 offset:32256
	ds_read_b128 v[194:197], v124 offset:32288
	ds_read_b128 v[198:201], v124 offset:18496
	ds_read_b128 v[202:205], v124 offset:18528
	ds_read_b128 v[206:209], v124 offset:27712
	ds_read_b128 v[100:103], v124 offset:27744
	v_mfma_f32_32x32x16_f16 v[32:47], v[134:137], v[64:67], v[32:47]
	v_mfma_f32_32x32x16_f16 v[48:63], v[130:133], v[64:67], v[48:63]
	v_mfma_f32_32x32x16_f16 v[32:47], v[134:137], v[68:71], v[32:47]
	ds_read_b128 v[134:137], v124 offset:23104
	ds_read_b128 v[210:213], v124 offset:23136
	ds_read_b128 v[214:217], v124 offset:32320
	ds_read_b128 v[96:99], v124 offset:32352
	s_waitcnt vmcnt(7)
	ds_write_b128 v218, v[220:223] offset:18432
	s_waitcnt vmcnt(6)
	ds_write_b128 v218, v[224:227] offset:27648
	s_waitcnt vmcnt(5)
	ds_write_b128 v218, v[228:231]
	s_waitcnt vmcnt(4)
	ds_write_b128 v218, v[232:235] offset:4608
	s_waitcnt vmcnt(3)
	ds_write_b128 v218, v[236:239] offset:9216
	s_waitcnt vmcnt(2)
	ds_write_b128 v218, v[240:243] offset:13824
	s_waitcnt vmcnt(1)
	ds_write_b128 v218, v[244:247] offset:23040
	v_max_f32_e32 v116, v49, v49
	v_max_f32_e32 v117, v48, v48
	s_waitcnt lgkmcnt(14)
	v_mfma_f32_32x32x16_f16 v[32:47], v[142:145], v[64:67], v[32:47]
	v_max_f32_e32 v116, v117, v116
	v_max3_f32 v116, v116, v50, v51
	v_max3_f32 v116, v116, v52, v53
	v_max3_f32 v116, v116, v54, v55
	v_max3_f32 v116, v116, v56, v57
	v_max3_f32 v116, v116, v58, v59
	v_max3_f32 v116, v116, v60, v61
	v_max3_f32 v116, v116, v62, v63
	s_nop 3
	v_max3_f32 v116, v116, v32, v33
	v_max3_f32 v116, v116, v34, v35
	v_max3_f32 v116, v116, v36, v37
	v_max3_f32 v116, v116, v38, v39
	v_max3_f32 v116, v116, v40, v41
	v_max3_f32 v116, v116, v42, v43
	v_max3_f32 v116, v116, v44, v45
	v_max3_f32 v116, v116, v46, v47
	ds_bpermute_b32 v117, v107, v116
	s_waitcnt vmcnt(0)
	ds_write_b128 v218, v[248:251] offset:32256
	s_waitcnt lgkmcnt(0)
	s_barrier
	v_max3_f32 v116, v125, v116, v117
	v_sub_f32_e32 v117, v125, v116
	v_fmamk_f32 v119, v116, 0xb9b8aa3b, v122
	v_mul_f32_e32 v117, 0x39b8aa3b, v117
	v_fmamk_f32 v48, v48, 0x39b8aa3b, v119
	v_fmamk_f32 v49, v49, 0x39b8aa3b, v119
	v_fmamk_f32 v50, v50, 0x39b8aa3b, v119
	v_fmamk_f32 v51, v51, 0x39b8aa3b, v119
	v_fmamk_f32 v52, v52, 0x39b8aa3b, v119
	v_fmamk_f32 v53, v53, 0x39b8aa3b, v119
	v_fmamk_f32 v54, v54, 0x39b8aa3b, v119
	v_fmamk_f32 v55, v55, 0x39b8aa3b, v119
	v_exp_f32_e32 v118, v117
	v_exp_f32_e32 v117, v48
	v_exp_f32_e32 v140, v49
	v_exp_f32_e32 v124, v50
	v_exp_f32_e32 v125, v51
	v_exp_f32_e32 v130, v52
	v_exp_f32_e32 v131, v53
	v_exp_f32_e32 v132, v54
	v_exp_f32_e32 v133, v55
	v_cvt_f16_f32_e32 v141, v117
	v_cvt_f16_f32_e32 v142, v140
	v_mul_f32_e32 v30, v118, v30
	v_mul_f32_e32 v31, v118, v31
	v_mul_f32_e32 v28, v118, v28
	v_mul_f32_e32 v29, v118, v29
	v_mul_f32_e32 v26, v118, v26
	v_mul_f32_e32 v27, v118, v27
	v_mul_f32_e32 v24, v118, v24
	v_mul_f32_e32 v25, v118, v25
	v_mul_f32_e32 v22, v118, v22
	v_mul_f32_e32 v23, v118, v23
	v_mul_f32_e32 v20, v118, v20
	v_mul_f32_e32 v21, v118, v21
	v_mul_f32_e32 v18, v118, v18
	v_mul_f32_e32 v19, v118, v19
	v_mul_f32_e32 v16, v118, v16
	v_mul_f32_e32 v17, v118, v17
	v_mul_f32_e32 v14, v118, v14
	v_mul_f32_e32 v15, v118, v15
	v_mul_f32_e32 v12, v118, v12
	v_mul_f32_e32 v13, v118, v13
	v_mul_f32_e32 v10, v118, v10
	v_mul_f32_e32 v11, v118, v11
	v_mul_f32_e32 v8, v118, v8
	v_mul_f32_e32 v9, v118, v9
	v_mul_f32_e32 v6, v118, v6
	v_mul_f32_e32 v7, v118, v7
	v_mul_f32_e32 v4, v118, v4
	v_mul_f32_e32 v5, v118, v5
	v_mul_f32_e32 v2, v118, v2
	v_mul_f32_e32 v3, v118, v3
	v_mul_f32_e32 v0, v118, v0
	v_mul_f32_e32 v1, v118, v1
	v_cvt_pk_f16_f32 v48, v117, v140
	v_cvt_pk_f16_f32 v49, v124, v125
	v_cvt_pk_f16_f32 v50, v130, v131
	v_cvt_pk_f16_f32 v51, v132, v133
	v_cvt_f32_f16_e32 v52, v49
	v_cvt_f32_f16_sdwa v53, v49 dst_sel:DWORD dst_unused:UNUSED_PAD src0_sel:WORD_1
	v_mfma_f32_32x32x16_f16 v[16:31], v[174:177], v[48:51], v[16:31]
	v_cvt_f32_f16_e32 v54, v50
	v_cvt_f32_f16_sdwa v55, v50 dst_sel:DWORD dst_unused:UNUSED_PAD src0_sel:WORD_1
	v_cvt_f32_f16_e32 v138, v51
	v_cvt_f32_f16_sdwa v139, v51 dst_sel:DWORD dst_unused:UNUSED_PAD src0_sel:WORD_1
	v_cvt_f32_f16_e32 v141, v141
	v_cvt_f32_f16_e32 v142, v142
	v_sub_f32_e32 v52, v124, v52
	v_sub_f32_e32 v53, v125, v53
	v_mfma_f32_32x32x16_f16 v[0:15], v[170:173], v[48:51], v[0:15]
	v_add_f32_e64 v54, v130, -v54
	v_add_f32_e64 v55, v131, -v55
	v_add_f32_e64 v138, v132, -v138
	v_add_f32_e64 v139, v133, -v139
	v_cvt_pk_f16_f32 v53, v52, v53
	v_cvt_pk_f16_f32 v54, v54, v55
	v_cvt_pk_f16_f32 v55, v138, v139
	v_sub_f32_e32 v52, v117, v141
	v_sub_f32_e32 v138, v140, v142
	v_cvt_pk_f16_f32 v52, v52, v138
	v_fmamk_f32 v56, v56, 0x39b8aa3b, v119
	v_fmamk_f32 v57, v57, 0x39b8aa3b, v119
	v_mfma_f32_32x32x16_f16 v[16:31], v[174:177], v[52:55], v[16:31]
	v_fmamk_f32 v58, v58, 0x39b8aa3b, v119
	v_fmamk_f32 v59, v59, 0x39b8aa3b, v119
	v_exp_f32_e32 v138, v56
	v_exp_f32_e32 v139, v57
	v_exp_f32_e32 v56, v58
	v_exp_f32_e32 v57, v59
	v_cvt_f16_f32_e32 v141, v138
	v_mfma_f32_32x32x16_f16 v[0:15], v[170:173], v[52:55], v[0:15]
	v_fmamk_f32 v52, v60, 0x39b8aa3b, v119
	v_fmamk_f32 v53, v61, 0x39b8aa3b, v119
	v_fmamk_f32 v54, v62, 0x39b8aa3b, v119
	v_fmamk_f32 v55, v63, 0x39b8aa3b, v119
	v_exp_f32_e32 v58, v52
	v_exp_f32_e32 v59, v53
	v_exp_f32_e32 v60, v54
	v_mfma_f32_32x32x16_f16 v[16:31], v[182:185], v[48:51], v[16:31]
	v_exp_f32_e32 v61, v55
	v_cvt_f16_f32_e32 v142, v139
	v_cvt_f32_f16_e32 v141, v141
	v_fmamk_f32 v32, v32, 0x39b8aa3b, v119
	v_fmamk_f32 v33, v33, 0x39b8aa3b, v119
	v_cvt_f32_f16_e32 v142, v142
	v_fmamk_f32 v34, v34, 0x39b8aa3b, v119
	v_mfma_f32_32x32x16_f16 v[0:15], v[190:193], v[48:51], v[0:15]
	v_cvt_pk_f16_f32 v48, v138, v139
	v_cvt_pk_f16_f32 v49, v56, v57
	v_cvt_pk_f16_f32 v50, v58, v59
	v_cvt_pk_f16_f32 v51, v60, v61
	v_cvt_f32_f16_e32 v52, v49
	v_cvt_f32_f16_sdwa v53, v49 dst_sel:DWORD dst_unused:UNUSED_PAD src0_sel:WORD_1
	v_cvt_f32_f16_e32 v54, v50
	v_mfma_f32_32x32x16_f16 v[16:31], v[178:181], v[48:51], v[16:31]
	v_cvt_f32_f16_sdwa v55, v50 dst_sel:DWORD dst_unused:UNUSED_PAD src0_sel:WORD_1
	v_cvt_f32_f16_e32 v62, v51
	v_cvt_f32_f16_sdwa v63, v51 dst_sel:DWORD dst_unused:UNUSED_PAD src0_sel:WORD_1
	v_add_f32_e64 v52, v56, -v52
	v_add_f32_e64 v53, v57, -v53
	v_sub_f32_e32 v54, v58, v54
	v_sub_f32_e32 v55, v59, v55
	v_cvt_pk_f16_f32 v53, v52, v53
	v_sub_f32_e32 v62, v60, v62
	v_sub_f32_e32 v63, v61, v63
	v_mfma_f32_32x32x16_f16 v[0:15], v[126:129], v[48:51], v[0:15]
	v_cvt_pk_f16_f32 v54, v54, v55
	v_cvt_pk_f16_f32 v55, v62, v63
	v_sub_f32_e32 v52, v138, v141
	v_sub_f32_e32 v62, v139, v142
	v_cvt_pk_f16_f32 v52, v52, v62
	v_fmamk_f32 v35, v35, 0x39b8aa3b, v119
	v_fmamk_f32 v36, v36, 0x39b8aa3b, v119
	v_mfma_f32_32x32x16_f16 v[16:31], v[178:181], v[52:55], v[16:31]
	v_fmamk_f32 v37, v37, 0x39b8aa3b, v119
	v_fmamk_f32 v38, v38, 0x39b8aa3b, v119
	v_fmamk_f32 v39, v39, 0x39b8aa3b, v119
	v_fmamk_f32 v62, v40, 0x39b8aa3b, v119
	v_fmamk_f32 v63, v41, 0x39b8aa3b, v119
	v_exp_f32_e32 v40, v34
	v_exp_f32_e32 v41, v35
	v_mfma_f32_32x32x16_f16 v[0:15], v[126:129], v[52:55], v[0:15]
	v_exp_f32_e32 v126, v32
	v_exp_f32_e32 v127, v33
	v_exp_f32_e32 v52, v36
	v_exp_f32_e32 v53, v37
	v_exp_f32_e32 v54, v38
	v_exp_f32_e32 v55, v39
	v_cvt_f16_f32_e32 v128, v126
	v_mfma_f32_32x32x16_f16 v[16:31], v[186:189], v[48:51], v[16:31]
	v_cvt_f16_f32_e32 v129, v127
	v_cvt_pk_f16_f32 v32, v126, v127
	v_cvt_pk_f16_f32 v33, v40, v41
	v_cvt_pk_f16_f32 v34, v52, v53
	v_cvt_pk_f16_f32 v35, v54, v55
	v_cvt_f32_f16_e32 v36, v33
	v_cvt_f32_f16_sdwa v37, v33 dst_sel:DWORD dst_unused:UNUSED_PAD src0_sel:WORD_1
	v_mfma_f32_32x32x16_f16 v[0:15], v[194:197], v[48:51], v[0:15]
	v_cvt_f32_f16_e32 v38, v34
	v_cvt_f32_f16_sdwa v39, v34 dst_sel:DWORD dst_unused:UNUSED_PAD src0_sel:WORD_1
	v_cvt_f32_f16_e32 v48, v35
	v_cvt_f32_f16_sdwa v49, v35 dst_sel:DWORD dst_unused:UNUSED_PAD src0_sel:WORD_1
	v_cvt_f32_f16_e32 v50, v128
	v_cvt_f32_f16_e32 v51, v129
	v_sub_f32_e32 v36, v40, v36
	v_sub_f32_e32 v37, v41, v37
	v_mfma_f32_32x32x16_f16 v[16:31], v[198:201], v[32:35], v[16:31]
	v_add_f32_e64 v38, v52, -v38
	v_add_f32_e64 v39, v53, -v39
	v_add_f32_e64 v48, v54, -v48
	v_add_f32_e64 v49, v55, -v49
	v_cvt_pk_f16_f32 v37, v36, v37
	v_cvt_pk_f16_f32 v38, v38, v39
	v_cvt_pk_f16_f32 v39, v48, v49
	v_sub_f32_e32 v36, v126, v50
	v_sub_f32_e32 v48, v127, v51
	v_mfma_f32_32x32x16_f16 v[0:15], v[134:137], v[32:35], v[0:15]
	v_cvt_pk_f16_f32 v36, v36, v48
	v_exp_f32_e32 v50, v62
	v_exp_f32_e32 v51, v63
	v_fmamk_f32 v42, v42, 0x39b8aa3b, v119
	v_fmamk_f32 v43, v43, 0x39b8aa3b, v119
	v_fmamk_f32 v44, v44, 0x39b8aa3b, v119
	v_fmamk_f32 v45, v45, 0x39b8aa3b, v119
	v_mfma_f32_32x32x16_f16 v[16:31], v[198:201], v[36:39], v[16:31]
	v_fmamk_f32 v46, v46, 0x39b8aa3b, v119
	v_fmac_f32_e32 v119, 0x39b8aa3b, v47
	v_exp_f32_e32 v42, v42
	v_exp_f32_e32 v43, v43
	v_exp_f32_e32 v44, v44
	v_exp_f32_e32 v45, v45
	v_exp_f32_e32 v46, v46
	v_mfma_f32_32x32x16_f16 v[0:15], v[134:137], v[36:39], v[0:15]
	v_exp_f32_e32 v47, v119
	v_cvt_f16_f32_e32 v62, v50
	v_cvt_f16_f32_e32 v63, v51
	v_add_f32_e32 v48, 0, v117
	v_cvt_pk_f16_f32 v37, v42, v43
	v_cvt_pk_f16_f32 v38, v44, v45
	v_cvt_pk_f16_f32 v39, v46, v47
	v_mfma_f32_32x32x16_f16 v[16:31], v[206:209], v[32:35], v[16:31]
	v_add_f32_e32 v117, v48, v140
	v_cvt_f32_f16_e32 v48, v39
	v_cvt_f32_f16_sdwa v49, v39 dst_sel:DWORD dst_unused:UNUSED_PAD src0_sel:WORD_1
	v_cvt_f32_f16_e32 v62, v62
	v_cvt_f32_f16_e32 v63, v63
	v_add_f32_e32 v117, v117, v124
	v_cvt_pk_f16_f32 v36, v50, v51
	v_mfma_f32_32x32x16_f16 v[0:15], v[214:217], v[32:35], v[0:15]
	v_cvt_f32_f16_e32 v32, v37
	v_cvt_f32_f16_sdwa v33, v37 dst_sel:DWORD dst_unused:UNUSED_PAD src0_sel:WORD_1
	v_cvt_f32_f16_e32 v34, v38
	v_cvt_f32_f16_sdwa v35, v38 dst_sel:DWORD dst_unused:UNUSED_PAD src0_sel:WORD_1
	v_add_f32_e32 v117, v117, v125
	v_sub_f32_e32 v32, v42, v32
	v_sub_f32_e32 v33, v43, v33
	v_sub_f32_e32 v48, v46, v48
	v_sub_f32_e32 v49, v47, v49
	v_sub_f32_e32 v34, v44, v34
	v_sub_f32_e32 v35, v45, v35
	v_mfma_f32_32x32x16_f16 v[16:31], v[202:205], v[36:39], v[16:31]
	v_add_f32_e32 v117, v117, v130
	v_cvt_pk_f16_f32 v33, v32, v33
	v_cvt_pk_f16_f32 v34, v34, v35
	v_cvt_pk_f16_f32 v35, v48, v49
	v_sub_f32_e32 v32, v50, v62
	v_sub_f32_e32 v48, v51, v63
	v_cvt_pk_f16_f32 v32, v32, v48
	v_mfma_f32_32x32x16_f16 v[0:15], v[210:213], v[36:39], v[0:15]
	v_add_f32_e32 v48, v117, v131
	v_add_f32_e32 v48, v48, v132
	v_add_f32_e32 v48, v48, v133
	v_add_f32_e32 v48, v48, v138
	v_add_f32_e32 v48, v48, v139
	v_add_f32_e32 v48, v48, v56
	v_add_f32_e32 v48, v48, v57
	v_mfma_f32_32x32x16_f16 v[16:31], v[202:205], v[32:35], v[16:31]
	v_mfma_f32_32x32x16_f16 v[0:15], v[210:213], v[32:35], v[0:15]
	v_add_f32_e32 v32, v48, v58
	v_add_f32_e32 v32, v32, v59
	v_add_f32_e32 v32, v32, v60
	v_add_f32_e32 v32, v32, v61
	v_add_f32_e32 v32, v32, v126
	v_add_f32_e32 v32, v32, v127
	v_add_f32_e32 v32, v32, v40
	v_add_f32_e32 v32, v32, v41
	v_add_f32_e32 v32, v32, v52
	v_add_f32_e32 v32, v32, v53
	v_add_f32_e32 v32, v32, v54
	v_add_f32_e32 v32, v32, v55
	v_add_f32_e32 v32, v32, v50
	v_mfma_f32_32x32x16_f16 v[16:31], v[100:103], v[36:39], v[16:31]
	v_add_f32_e32 v32, v32, v51
	v_add_f32_e32 v32, v32, v42
	v_add_f32_e32 v32, v32, v43
	v_add_f32_e32 v32, v32, v44
	v_add_f32_e32 v32, v32, v45
	v_add_f32_e32 v32, v32, v46
	v_add_f32_e32 v100, v32, v47
	v_mfma_f32_32x32x16_f16 v[0:15], v[96:99], v[36:39], v[0:15]
	v_fmac_f32_e32 v100, v123, v118
	s_cbranch_scc0 .LBB2_1
	ds_read_b128 v[48:51], v120 offset:36864
	ds_read_b128 v[52:55], v120 offset:36896
	v_add_u32_e32 v102, 0xea00, v120
	s_ashr_i32 s0, s0, 3
	s_ashr_i32 s1, s0, 31
	s_waitcnt lgkmcnt(1)
	v_mfma_f32_32x32x16_f16 v[32:47], v[48:51], v[88:91], 0
	s_lshl_b64 s[0:1], s[0:1], 10
	v_mfma_f32_32x32x16_f16 v[32:47], v[48:51], v[92:95], v[32:47]
	ds_read_b128 v[48:51], v120 offset:46080
	ds_read_b128 v[56:59], v120 offset:46112
	s_waitcnt lgkmcnt(1)
	v_mfma_f32_32x32x16_f16 v[32:47], v[48:51], v[88:91], v[32:47]
	v_mfma_f32_32x32x16_f16 v[32:47], v[52:55], v[80:83], v[32:47]
	v_mfma_f32_32x32x16_f16 v[32:47], v[52:55], v[84:87], v[32:47]
	ds_read_b128 v[48:51], v120 offset:36928
	ds_read_b128 v[52:55], v120 offset:36960
	s_waitcnt lgkmcnt(2)
	v_mfma_f32_32x32x16_f16 v[32:47], v[56:59], v[80:83], v[32:47]
	s_waitcnt lgkmcnt(1)
	v_mfma_f32_32x32x16_f16 v[32:47], v[48:51], v[72:75], v[32:47]
	v_mfma_f32_32x32x16_f16 v[32:47], v[48:51], v[76:79], v[32:47]
	ds_read_b128 v[48:51], v120 offset:46144
	ds_read_b128 v[56:59], v120 offset:46176
	ds_read_b128 v[96:99], v120 offset:41472
	ds_read_b128 v[108:111], v120 offset:41504
	s_waitcnt lgkmcnt(3)
	v_mfma_f32_32x32x16_f16 v[32:47], v[48:51], v[72:75], v[32:47]
	v_mfma_f32_32x32x16_f16 v[32:47], v[52:55], v[64:67], v[32:47]
	v_mfma_f32_32x32x16_f16 v[32:47], v[52:55], v[68:71], v[32:47]
	s_waitcnt lgkmcnt(2)
	v_mfma_f32_32x32x16_f16 v[32:47], v[56:59], v[64:67], v[32:47]
	s_waitcnt lgkmcnt(1)
	v_mfma_f32_32x32x16_f16 v[48:63], v[96:99], v[88:91], 0
	v_mfma_f32_32x32x16_f16 v[48:63], v[96:99], v[92:95], v[48:63]
	ds_read_b128 v[92:95], v120 offset:50688
	ds_read_b128 v[96:99], v120 offset:50720
	s_waitcnt lgkmcnt(1)
	v_mfma_f32_32x32x16_f16 v[48:63], v[92:95], v[88:91], v[48:63]
	v_mfma_f32_32x32x16_f16 v[48:63], v[108:111], v[80:83], v[48:63]
	v_mfma_f32_32x32x16_f16 v[48:63], v[108:111], v[84:87], v[48:63]
	s_waitcnt lgkmcnt(0)
	v_mfma_f32_32x32x16_f16 v[48:63], v[96:99], v[80:83], v[48:63]
	ds_read_b128 v[80:83], v120 offset:41536
	ds_read_b128 v[84:87], v120 offset:41568
	s_waitcnt lgkmcnt(1)
	v_mfma_f32_32x32x16_f16 v[48:63], v[80:83], v[72:75], v[48:63]
	v_mfma_f32_32x32x16_f16 v[48:63], v[80:83], v[76:79], v[48:63]
	ds_read_b128 v[76:79], v120 offset:50752
	ds_read_b128 v[80:83], v120 offset:50784
	s_waitcnt lgkmcnt(1)
	v_mfma_f32_32x32x16_f16 v[48:63], v[76:79], v[72:75], v[48:63]
	v_max_f32_e32 v72, v33, v33
	v_max_f32_e32 v73, v32, v32
	v_max_f32_e32 v72, v73, v72
	v_mfma_f32_32x32x16_f16 v[48:63], v[84:87], v[64:67], v[48:63]
	v_mfma_f32_32x32x16_f16 v[48:63], v[84:87], v[68:71], v[48:63]
	v_max3_f32 v68, v72, v34, v35
	v_max3_f32 v68, v68, v36, v37
	v_max3_f32 v68, v68, v38, v39
	v_max3_f32 v68, v68, v40, v41
	v_max3_f32 v68, v68, v42, v43
	v_max3_f32 v68, v68, v44, v45
	v_max3_f32 v68, v68, v46, v47
	s_waitcnt lgkmcnt(0)
	v_mfma_f32_32x32x16_f16 v[48:63], v[80:83], v[64:67], v[48:63]
	s_nop 11
	v_max3_f32 v64, v68, v48, v49
	v_max3_f32 v64, v64, v50, v51
	v_max3_f32 v64, v64, v52, v53
	v_max3_f32 v64, v64, v54, v55
	v_max3_f32 v64, v64, v56, v57
	v_max3_f32 v64, v64, v58, v59
	v_max3_f32 v64, v64, v60, v61
	v_max3_f32 v64, v64, v62, v63
	ds_bpermute_b32 v65, v107, v64
	v_mov_b32_e32 v68, 0x41000000
	s_waitcnt lgkmcnt(0)
	v_max3_f32 v65, v116, v64, v65
	v_fmac_f32_e32 v68, 0xb9b8aa3b, v65
	v_fmamk_f32 v32, v32, 0x39b8aa3b, v68
	v_sub_f32_e32 v64, v116, v65
	v_exp_f32_e32 v65, v32
	v_fmamk_f32 v32, v33, 0x39b8aa3b, v68
	v_exp_f32_e32 v101, v32
	v_fmamk_f32 v32, v34, 0x39b8aa3b, v68
	v_exp_f32_e32 v66, v32
	v_fmamk_f32 v32, v35, 0x39b8aa3b, v68
	v_exp_f32_e32 v67, v32
	v_fmamk_f32 v32, v36, 0x39b8aa3b, v68
	v_exp_f32_e32 v36, v32
	v_fmamk_f32 v32, v37, 0x39b8aa3b, v68
	v_exp_f32_e32 v37, v32
	v_fmamk_f32 v32, v38, 0x39b8aa3b, v68
	v_exp_f32_e32 v38, v32
	v_fmamk_f32 v32, v39, 0x39b8aa3b, v68
	v_exp_f32_e32 v39, v32
	v_fmamk_f32 v32, v40, 0x39b8aa3b, v68
	v_exp_f32_e32 v124, v32
	v_fmamk_f32 v32, v41, 0x39b8aa3b, v68
	v_exp_f32_e32 v125, v32
	v_fmamk_f32 v32, v42, 0x39b8aa3b, v68
	v_exp_f32_e32 v40, v32
	v_fmamk_f32 v32, v43, 0x39b8aa3b, v68
	v_exp_f32_e32 v41, v32
	v_fmamk_f32 v32, v44, 0x39b8aa3b, v68
	v_exp_f32_e32 v42, v32
	v_fmamk_f32 v32, v45, 0x39b8aa3b, v68
	v_exp_f32_e32 v43, v32
	v_fmamk_f32 v32, v46, 0x39b8aa3b, v68
	v_exp_f32_e32 v44, v32
	v_fmamk_f32 v32, v47, 0x39b8aa3b, v68
	v_exp_f32_e32 v45, v32
	v_fmamk_f32 v32, v48, 0x39b8aa3b, v68
	v_exp_f32_e32 v126, v32
	v_fmamk_f32 v32, v49, 0x39b8aa3b, v68
	v_exp_f32_e32 v127, v32
	v_fmamk_f32 v32, v50, 0x39b8aa3b, v68
	v_exp_f32_e32 v46, v32
	v_fmamk_f32 v32, v51, 0x39b8aa3b, v68
	v_exp_f32_e32 v47, v32
	v_fmamk_f32 v32, v52, 0x39b8aa3b, v68
	v_exp_f32_e32 v48, v32
	v_fmamk_f32 v32, v53, 0x39b8aa3b, v68
	v_exp_f32_e32 v49, v32
	v_fmamk_f32 v32, v54, 0x39b8aa3b, v68
	v_exp_f32_e32 v50, v32
	v_fmamk_f32 v32, v55, 0x39b8aa3b, v68
	v_exp_f32_e32 v51, v32
	v_fmamk_f32 v32, v56, 0x39b8aa3b, v68
	v_exp_f32_e32 v128, v32
	v_fmamk_f32 v32, v57, 0x39b8aa3b, v68
	v_exp_f32_e32 v129, v32
	v_fmamk_f32 v32, v58, 0x39b8aa3b, v68
	v_exp_f32_e32 v52, v32
	v_fmamk_f32 v32, v59, 0x39b8aa3b, v68
	v_exp_f32_e32 v53, v32
	v_fmamk_f32 v32, v60, 0x39b8aa3b, v68
	v_exp_f32_e32 v54, v32
	v_fmamk_f32 v32, v61, 0x39b8aa3b, v68
	v_exp_f32_e32 v55, v32
	v_fmamk_f32 v32, v62, 0x39b8aa3b, v68
	v_exp_f32_e32 v56, v32
	v_cvt_f16_f32_e32 v32, v65
	v_cvt_f16_f32_e32 v33, v101
	v_cvt_pk_f16_f32 v59, v66, v67
	v_cvt_pk_f16_f32 v60, v36, v37
	v_cvt_f32_f16_e32 v32, v32
	v_cvt_f32_f16_e32 v35, v33
	v_cvt_f32_f16_sdwa v33, v59 dst_sel:DWORD dst_unused:UNUSED_PAD src0_sel:WORD_1
	v_fmac_f32_e32 v68, 0x39b8aa3b, v63
	v_sub_f32_e32 v34, v65, v32
	v_cvt_f32_f16_e32 v32, v59
	v_sub_f32_e32 v35, v101, v35
	v_cvt_pk_f16_f32 v61, v38, v39
	v_exp_f32_e32 v57, v68
	v_pk_add_f32 v[32:33], v[66:67], v[32:33] neg_lo:[0,1] neg_hi:[0,1]
	v_cvt_pk_f16_f32 v68, v34, v35
	v_cvt_pk_f16_f32 v69, v32, v33
	v_cvt_f32_f16_e32 v32, v60
	v_cvt_f32_f16_sdwa v33, v60 dst_sel:DWORD dst_unused:UNUSED_PAD src0_sel:WORD_1
	v_cvt_f32_f16_e32 v34, v61
	v_cvt_f32_f16_sdwa v35, v61 dst_sel:DWORD dst_unused:UNUSED_PAD src0_sel:WORD_1
	v_mul_f32_e32 v64, 0x39b8aa3b, v64
	v_pk_add_f32 v[32:33], v[36:37], v[32:33] neg_lo:[0,1] neg_hi:[0,1]
	v_exp_f32_e32 v64, v64
	v_cvt_pk_f16_f32 v70, v32, v33
	v_pk_add_f32 v[32:33], v[38:39], v[34:35] neg_lo:[0,1] neg_hi:[0,1]
	v_cvt_f16_f32_e32 v62, v124
	v_cvt_pk_f16_f32 v71, v32, v33
	ds_read_b128 v[32:35], v120 offset:55296
	v_cvt_f16_f32_e32 v63, v125
	v_pk_mul_f32 v[30:31], v[64:65], v[30:31] op_sel_hi:[0,1]
	v_pk_mul_f32 v[28:29], v[64:65], v[28:29] op_sel_hi:[0,1]
	v_pk_mul_f32 v[26:27], v[64:65], v[26:27] op_sel_hi:[0,1]
	v_pk_mul_f32 v[24:25], v[64:65], v[24:25] op_sel_hi:[0,1]
	v_pk_mul_f32 v[22:23], v[64:65], v[22:23] op_sel_hi:[0,1]
	v_pk_mul_f32 v[20:21], v[64:65], v[20:21] op_sel_hi:[0,1]
	v_pk_mul_f32 v[18:19], v[64:65], v[18:19] op_sel_hi:[0,1]
	v_pk_mul_f32 v[16:17], v[64:65], v[16:17] op_sel_hi:[0,1]
	v_cvt_pk_f16_f32 v58, v65, v101
	v_cvt_f32_f16_e32 v62, v62
	v_cvt_f32_f16_e32 v75, v63
	s_waitcnt lgkmcnt(0)
	v_mfma_f32_32x32x16_f16 v[16:31], v[32:35], v[58:61], v[16:31]
	v_cvt_pk_f16_f32 v73, v40, v41
	v_sub_f32_e32 v74, v124, v62
	v_sub_f32_e32 v75, v125, v75
	v_cvt_f32_f16_e32 v62, v73
	v_cvt_f32_f16_sdwa v63, v73 dst_sel:DWORD dst_unused:UNUSED_PAD src0_sel:WORD_1
	v_cvt_pk_f16_f32 v76, v74, v75
	v_cvt_pk_f16_f32 v74, v42, v43
	v_cvt_f32_f16_e32 v78, v74
	v_cvt_f32_f16_sdwa v79, v74 dst_sel:DWORD dst_unused:UNUSED_PAD src0_sel:WORD_1
	v_cvt_pk_f16_f32 v75, v44, v45
	v_cvt_f32_f16_e32 v80, v75
	v_cvt_f32_f16_sdwa v81, v75 dst_sel:DWORD dst_unused:UNUSED_PAD src0_sel:WORD_1
	v_mfma_f32_32x32x16_f16 v[16:31], v[32:35], v[68:71], v[16:31]
	v_add_f32_e64 v62, v40, -v62
	v_add_f32_e64 v63, v41, -v63
	v_mul_f32_e64 v14, v64, v14
	v_mul_f32_e64 v15, v64, v15
	v_cvt_pk_f16_f32 v77, v62, v63
	v_pk_add_f32 v[62:63], v[42:43], v[78:79] neg_lo:[0,1] neg_hi:[0,1]
	v_pk_mul_f32 v[12:13], v[64:65], v[12:13] op_sel_hi:[0,1]
	v_cvt_pk_f16_f32 v78, v62, v63
	v_pk_add_f32 v[62:63], v[44:45], v[80:81] neg_lo:[0,1] neg_hi:[0,1]
	ds_read_b128 v[80:83], v120 offset:55328
	ds_read_b128 v[84:87], v120 offset:64512
	ds_read_b128 v[88:91], v120 offset:64544
	s_waitcnt lgkmcnt(1)
	v_mfma_f32_32x32x16_f16 v[16:31], v[84:87], v[58:61], v[16:31]
	ds_read_b128 v[92:95], v120 offset:59904
	ds_read_b128 v[96:99], v120 offset:59936
	v_cvt_pk_f16_f32 v79, v62, v63
	v_add_u32_e32 v63, 0xea20, v120
	v_cvt_f16_f32_e32 v62, v126
	ds_read_b128 v[108:111], v102 offset:9216
	ds_read_b128 v[112:115], v63 offset:9216
	v_cvt_f16_f32_e32 v63, v127
	v_pk_mul_f32 v[10:11], v[64:65], v[10:11] op_sel_hi:[0,1]
	v_pk_mul_f32 v[8:9], v[64:65], v[8:9] op_sel_hi:[0,1]
	v_pk_mul_f32 v[6:7], v[64:65], v[6:7] op_sel_hi:[0,1]
	v_pk_mul_f32 v[4:5], v[64:65], v[4:5] op_sel_hi:[0,1]
	v_pk_mul_f32 v[2:3], v[64:65], v[2:3] op_sel_hi:[0,1]
	v_pk_mul_f32 v[0:1], v[64:65], v[0:1] op_sel_hi:[0,1]
	v_cvt_pk_f16_f32 v33, v46, v47
	v_cvt_f32_f16_e32 v34, v33
	s_waitcnt lgkmcnt(3)
	v_mfma_f32_32x32x16_f16 v[0:15], v[92:95], v[58:61], v[0:15]
	v_cvt_f32_f16_sdwa v35, v33 dst_sel:DWORD dst_unused:UNUSED_PAD src0_sel:WORD_1
	v_cvt_pk_f16_f32 v72, v124, v125
	v_cvt_f32_f16_e32 v62, v62
	v_cvt_f32_f16_e32 v63, v63
	v_add_f32_e64 v34, v46, -v34
	v_add_f32_e64 v35, v47, -v35
	v_cvt_f16_f32_e32 v87, v128
	v_sub_f32_e32 v62, v126, v62
	v_mfma_f32_32x32x16_f16 v[16:31], v[80:83], v[72:75], v[16:31]
	v_sub_f32_e32 v63, v127, v63
	v_cvt_pk_f16_f32 v85, v34, v35
	v_cvt_pk_f16_f32 v34, v48, v49
	v_cvt_pk_f16_f32 v84, v62, v63
	v_cvt_f32_f16_e32 v62, v34
	v_cvt_f32_f16_sdwa v63, v34 dst_sel:DWORD dst_unused:UNUSED_PAD src0_sel:WORD_1
	v_cvt_pk_f16_f32 v35, v50, v51
	v_cvt_f32_f16_e32 v102, v35
	v_cvt_f32_f16_sdwa v103, v35 dst_sel:DWORD dst_unused:UNUSED_PAD src0_sel:WORD_1
	v_mfma_f32_32x32x16_f16 v[0:15], v[92:95], v[68:71], v[0:15]
	v_cvt_f16_f32_e32 v68, v129
	v_add_f32_e64 v62, v48, -v62
	v_add_f32_e64 v63, v49, -v63
	v_cvt_pk_f16_f32 v69, v52, v53
	v_cvt_pk_f16_f32 v86, v62, v63
	v_pk_add_f32 v[62:63], v[50:51], v[102:103] neg_lo:[0,1] neg_hi:[0,1]
	v_cvt_f32_f16_e32 v102, v87
	v_cvt_f32_f16_e32 v71, v68
	v_mfma_f32_32x32x16_f16 v[16:31], v[80:83], v[76:79], v[16:31]
	v_cvt_pk_f16_f32 v87, v62, v63
	v_cvt_f32_f16_e32 v62, v69
	v_cvt_f32_f16_sdwa v63, v69 dst_sel:DWORD dst_unused:UNUSED_PAD src0_sel:WORD_1
	v_sub_f32_e32 v70, v128, v102
	v_cvt_pk_f16_f32 v32, v126, v127
	v_add_u32_e32 v103, 0xea40, v120
	v_cvt_pk_f16_f32 v68, v128, v129
	s_waitcnt lgkmcnt(1)
	v_mfma_f32_32x32x16_f16 v[0:15], v[108:111], v[58:61], v[0:15]
	v_sub_f32_e32 v58, v129, v71
	v_cvt_pk_f16_f32 v58, v70, v58
	v_add_f32_e64 v60, v52, -v62
	v_add_f32_e64 v61, v53, -v63
	v_cvt_pk_f16_f32 v70, v54, v55
	v_cvt_pk_f16_f32 v71, v56, v57
	v_cvt_pk_f16_f32 v59, v60, v61
	v_cvt_f32_f16_e32 v60, v70
	v_cvt_f32_f16_sdwa v61, v70 dst_sel:DWORD dst_unused:UNUSED_PAD src0_sel:WORD_1
	v_cvt_f32_f16_e32 v62, v71
	v_cvt_f32_f16_sdwa v63, v71 dst_sel:DWORD dst_unused:UNUSED_PAD src0_sel:WORD_1
	v_mfma_f32_32x32x16_f16 v[16:31], v[88:91], v[72:75], v[16:31]
	v_add_f32_e64 v60, v54, -v60
	v_add_f32_e64 v61, v55, -v61
	ds_read_b128 v[80:83], v120 offset:55360
	ds_read_b128 v[92:95], v120 offset:55392
	ds_read_b128 v[108:111], v120 offset:64576
	ds_read_b128 v[116:119], v120 offset:64608
	v_pk_add_f32 v[62:63], v[56:57], v[62:63] neg_lo:[0,1] neg_hi:[0,1]
	v_cvt_pk_f16_f32 v60, v60, v61
	v_cvt_pk_f16_f32 v61, v62, v63
	v_add_f32_e32 v63, 0, v65
	v_add_f32_e32 v63, v63, v101
	v_add_f32_e32 v63, v63, v66
	v_add_f32_e32 v63, v63, v67
	v_add_f32_e32 v36, v63, v36
	s_waitcnt lgkmcnt(3)
	v_mfma_f32_32x32x16_f16 v[16:31], v[80:83], v[32:35], v[16:31]
	v_add_f32_e32 v36, v36, v37
	v_add_f32_e32 v36, v36, v38
	v_add_f32_e32 v36, v36, v39
	v_add_f32_e32 v36, v36, v124
	v_add_f32_e32 v36, v36, v125
	v_add_f32_e32 v36, v36, v40
	v_add_f32_e32 v36, v36, v41
	v_mfma_f32_32x32x16_f16 v[0:15], v[96:99], v[72:75], v[0:15]
	v_add_f32_e32 v36, v36, v42
	v_add_f32_e32 v36, v36, v43
	v_add_f32_e32 v36, v36, v44
	v_add_f32_e32 v36, v36, v45
	v_add_f32_e32 v36, v36, v126
	v_add_f32_e32 v36, v36, v127
	v_add_f32_e32 v36, v36, v46
	v_mfma_f32_32x32x16_f16 v[16:31], v[80:83], v[84:87], v[16:31]
	v_add_f32_e32 v36, v36, v47
	v_add_f32_e32 v36, v36, v48
	v_add_f32_e32 v36, v36, v49
	v_add_f32_e32 v36, v36, v50
	v_add_f32_e32 v36, v36, v51
	v_add_f32_e32 v36, v36, v128
	v_add_f32_e32 v36, v36, v129
	v_mfma_f32_32x32x16_f16 v[0:15], v[96:99], v[76:79], v[0:15]
	v_add_f32_e32 v36, v36, v52
	v_add_u32_e32 v62, 0xea60, v120
	ds_read_b128 v[88:91], v120 offset:59968
	ds_read_b128 v[120:123], v120 offset:60000
	v_add_f32_e32 v36, v36, v53
	v_add_f32_e32 v36, v36, v54
	v_add_f32_e32 v36, v36, v55
	v_add_f32_e32 v36, v36, v56
	s_waitcnt lgkmcnt(3)
	v_mfma_f32_32x32x16_f16 v[16:31], v[108:111], v[32:35], v[16:31]
	v_add_f32_e32 v44, v36, v57
	v_fmac_f32_e32 v44, v100, v64
	ds_bpermute_b32 v45, v107, v44
	ds_read_b128 v[36:39], v103 offset:9216
	ds_read_b128 v[40:43], v62 offset:9216
	s_waitcnt lgkmcnt(0)
	s_barrier
	v_mfma_f32_32x32x16_f16 v[0:15], v[112:115], v[72:75], v[0:15]
	v_add_f32_e32 v44, v44, v45
	v_div_scale_f32 v45, s[4:5], v44, v44, 4.0
	v_rcp_f32_e32 v46, v45
	s_nop 0
	v_fma_f32 v47, -v45, v46, 1.0
	v_mfma_f32_32x32x16_f16 v[16:31], v[92:95], v[68:71], v[16:31]
	v_fmac_f32_e32 v46, v47, v46
	v_div_scale_f32 v47, vcc, 4.0, v44, 4.0
	v_mul_f32_e32 v48, v47, v46
	v_fma_f32 v49, -v45, v48, v47
	v_fmac_f32_e32 v48, v49, v46
	v_fma_f32 v45, -v45, v48, v47
	v_mfma_f32_32x32x16_f16 v[0:15], v[88:91], v[32:35], v[0:15]
	v_div_fmas_f32 v45, v45, v46, v48
	v_div_fixup_f32 v44, v45, v44, 4.0
	v_or3_b32 v47, s1, 0, 0
	v_or3_b32 v46, s0, v106, v104
	s_lshl_b32 s0, s2, 7
	v_lshlrev_b64 v[46:47], 10, v[46:47]
	s_and_b32 s0, s0, 0x380
	v_mfma_f32_32x32x16_f16 v[16:31], v[92:95], v[58:61], v[16:31]
	v_or_b32_e32 v46, s0, v46
	v_lshl_add_u64 v[48:49], s[8:9], 0, v[46:47]
	v_lshl_add_u64 v[46:47], s[10:11], 0, v[46:47]
	v_mfma_f32_32x32x16_f16 v[0:15], v[88:91], v[84:87], v[0:15]
	v_mfma_f32_32x32x16_f16 v[16:31], v[116:119], v[68:71], v[16:31]
	v_mfma_f32_32x32x16_f16 v[0:15], v[36:39], v[32:35], v[0:15]
	s_nop 10
	v_mul_f32_e32 v45, v44, v16
	v_fma_mixlo_f16 v50, v44, v16, 0
	v_fma_mixlo_f16 v16, v44, v16, -v50 op_sel_hi:[0,0,1]
	v_mul_f32_e64 v50, v44, v18
	v_mul_f32_e64 v51, v44, v19
	v_cvt_pk_f16_f32 v51, v50, v51
	v_cvt_f32_f16_e32 v52, v51
	v_cvt_f32_f16_sdwa v53, v51 dst_sel:DWORD dst_unused:UNUSED_PAD src0_sel:WORD_1
	v_mfma_f32_32x32x16_f16 v[0:15], v[120:123], v[68:71], v[0:15]
	v_mul_f32_e64 v32, v44, v22
	v_mul_f32_e64 v33, v44, v23
	v_fma_mixlo_f16 v55, v44, v17, 0
	v_fma_f32 v18, v44, v18, -v52
	v_fma_f32 v19, v44, v19, -v53
	v_cvt_pk_f16_f32 v33, v32, v33
	v_mul_f32_e32 v54, v44, v17
	v_fma_mixhi_f16 v16, v44, v17, -v55 op_sel_hi:[0,0,1]
	v_cvt_pk_f16_f32 v17, v18, v19
	v_lshlrev_b32_e32 v18, 3, v105
	v_mov_b32_e32 v19, 0
	v_cvt_f32_f16_e32 v34, v33
	v_cvt_f32_f16_sdwa v35, v33 dst_sel:DWORD dst_unused:UNUSED_PAD src0_sel:WORD_1
	v_lshl_add_u64 v[48:49], v[48:49], 0, v[18:19]
	v_lshl_add_u64 v[18:19], v[46:47], 0, v[18:19]
	global_store_dwordx2 v[18:19], v[16:17], off
	v_fma_mixlo_f16 v16, v44, v20, 0
	v_mul_f32_e32 v17, v44, v20
	v_fma_mixlo_f16 v16, v44, v20, -v16 op_sel_hi:[0,0,1]
	v_mul_f32_e32 v20, v44, v21
	v_fma_mixlo_f16 v36, v44, v21, 0
	v_mfma_f32_32x32x16_f16 v[0:15], v[120:123], v[58:61], v[0:15]
	v_cvt_pk_f16_f32 v32, v17, v20
	v_fma_mixhi_f16 v16, v44, v21, -v36 op_sel_hi:[0,0,1]
	v_fma_f32 v20, v44, v22, -v34
	v_fma_f32 v21, v44, v23, -v35
	v_cvt_pk_f16_f32 v17, v20, v21
	v_pk_mul_f32 v[20:21], v[44:45], v[26:27] op_sel_hi:[0,1]
	v_cvt_pk_f16_f32 v21, v20, v21
	v_cvt_f32_f16_e32 v22, v21
	v_cvt_f32_f16_sdwa v23, v21 dst_sel:DWORD dst_unused:UNUSED_PAD src0_sel:WORD_1
	v_cvt_pk_f16_f32 v50, v45, v54
	global_store_dwordx2 v[48:49], v[50:51], off
	global_store_dwordx2 v[48:49], v[32:33], off offset:16
	global_store_dwordx2 v[18:19], v[16:17], off offset:16
	v_fma_mixlo_f16 v16, v44, v24, 0
	v_mul_f32_e32 v17, v44, v24
	v_fma_mixlo_f16 v16, v44, v24, -v16 op_sel_hi:[0,0,1]
	v_mul_f32_e32 v24, v44, v25
	v_mfma_f32_32x32x16_f16 v[0:15], v[40:43], v[68:71], v[0:15]
	v_fma_mixlo_f16 v32, v44, v25, 0
	v_cvt_pk_f16_f32 v20, v17, v24
	v_fma_f32 v22, v44, v26, -v22
	v_fma_f32 v23, v44, v27, -v23
	v_fma_mixhi_f16 v16, v44, v25, -v32 op_sel_hi:[0,0,1]
	v_cvt_pk_f16_f32 v17, v22, v23
	global_store_dwordx2 v[48:49], v[20:21], off offset:32
	global_store_dwordx2 v[18:19], v[16:17], off offset:32
	v_pk_mul_f32 v[20:21], v[44:45], v[30:31] op_sel_hi:[0,1]
	v_cvt_pk_f16_f32 v21, v20, v21
	v_cvt_f32_f16_e32 v22, v21
	v_cvt_f32_f16_sdwa v23, v21 dst_sel:DWORD dst_unused:UNUSED_PAD src0_sel:WORD_1
	v_fma_mixlo_f16 v16, v44, v28, 0
	v_mul_f32_e32 v17, v44, v28
	v_fma_mixlo_f16 v16, v44, v28, -v16 op_sel_hi:[0,0,1]
	v_mul_f32_e32 v24, v44, v29
	v_fma_mixlo_f16 v25, v44, v29, 0
	v_cvt_pk_f16_f32 v20, v17, v24
	v_fma_mixhi_f16 v16, v44, v29, -v25 op_sel_hi:[0,0,1]
	v_pk_fma_f32 v[22:23], v[44:45], v[30:31], v[22:23] op_sel_hi:[0,1,1] neg_lo:[0,0,1] neg_hi:[0,0,1]
	v_cvt_pk_f16_f32 v17, v22, v23
	global_store_dwordx2 v[48:49], v[20:21], off offset:48
	global_store_dwordx2 v[18:19], v[16:17], off offset:48
	v_fma_mixlo_f16 v16, v44, v0, 0
	v_mul_f32_e32 v22, v44, v0
	v_fma_mixlo_f16 v0, v44, v0, -v16 op_sel_hi:[0,0,1]
	v_pk_mul_f32 v[16:17], v[44:45], v[2:3] op_sel_hi:[0,1]
	v_cvt_pk_f16_f32 v17, v16, v17
	v_cvt_f32_f16_e32 v20, v17
	v_cvt_f32_f16_sdwa v21, v17 dst_sel:DWORD dst_unused:UNUSED_PAD src0_sel:WORD_1
	v_fma_mixlo_f16 v24, v44, v1, 0
	v_mul_f32_e32 v23, v44, v1
	v_fma_mixhi_f16 v0, v44, v1, -v24 op_sel_hi:[0,0,1]
	v_pk_fma_f32 v[2:3], v[44:45], v[2:3], v[20:21] op_sel_hi:[0,1,1] neg_lo:[0,0,1] neg_hi:[0,0,1]
	v_cvt_pk_f16_f32 v1, v2, v3
	v_pk_mul_f32 v[2:3], v[44:45], v[6:7] op_sel_hi:[0,1]
	v_cvt_pk_f16_f32 v16, v22, v23
	v_cvt_pk_f16_f32 v3, v2, v3
	global_store_dwordx2 v[48:49], v[16:17], off offset:64
	global_store_dwordx2 v[18:19], v[0:1], off offset:64
	v_cvt_f32_f16_e32 v16, v3
	v_cvt_f32_f16_sdwa v17, v3 dst_sel:DWORD dst_unused:UNUSED_PAD src0_sel:WORD_1
	v_fma_mixlo_f16 v0, v44, v4, 0
	v_mul_f32_e32 v1, v44, v4
	v_fma_mixlo_f16 v0, v44, v4, -v0 op_sel_hi:[0,0,1]
	v_mul_f32_e32 v4, v44, v5
	v_fma_mixlo_f16 v20, v44, v5, 0
	v_cvt_pk_f16_f32 v2, v1, v4
	v_fma_mixhi_f16 v0, v44, v5, -v20 op_sel_hi:[0,0,1]
	v_pk_fma_f32 v[4:5], v[44:45], v[6:7], v[16:17] op_sel_hi:[0,1,1] neg_lo:[0,0,1] neg_hi:[0,0,1]
	v_cvt_pk_f16_f32 v1, v4, v5
	global_store_dwordx2 v[48:49], v[2:3], off offset:80
	global_store_dwordx2 v[18:19], v[0:1], off offset:80
	v_pk_mul_f32 v[2:3], v[44:45], v[10:11] op_sel_hi:[0,1]
	v_cvt_pk_f16_f32 v3, v2, v3
	v_cvt_f32_f16_e32 v4, v3
	v_cvt_f32_f16_sdwa v5, v3 dst_sel:DWORD dst_unused:UNUSED_PAD src0_sel:WORD_1
	v_mul_f32_e32 v1, v44, v8
	v_fma_mixlo_f16 v0, v44, v8, 0
	v_mul_f32_e32 v6, v44, v9
	v_fma_mixlo_f16 v0, v44, v8, -v0 op_sel_hi:[0,0,1]
	v_fma_mixlo_f16 v7, v44, v9, 0
	v_cvt_pk_f16_f32 v2, v1, v6
	v_pk_fma_f32 v[4:5], v[44:45], v[10:11], v[4:5] op_sel_hi:[0,1,1] neg_lo:[0,0,1] neg_hi:[0,0,1]
	v_fma_mixhi_f16 v0, v44, v9, -v7 op_sel_hi:[0,0,1]
	v_cvt_pk_f16_f32 v1, v4, v5
	global_store_dwordx2 v[48:49], v[2:3], off offset:96
	global_store_dwordx2 v[18:19], v[0:1], off offset:96
	v_pk_mul_f32 v[2:3], v[44:45], v[14:15] op_sel_hi:[0,1]
	v_cvt_pk_f16_f32 v3, v2, v3
	v_cvt_f32_f16_e32 v4, v3
	v_cvt_f32_f16_sdwa v5, v3 dst_sel:DWORD dst_unused:UNUSED_PAD src0_sel:WORD_1
	v_mul_f32_e32 v1, v44, v12
	v_fma_mixlo_f16 v0, v44, v12, 0
	v_mul_f32_e32 v6, v44, v13
	v_fma_mixlo_f16 v0, v44, v12, -v0 op_sel_hi:[0,0,1]
	v_fma_mixlo_f16 v7, v44, v13, 0
	v_cvt_pk_f16_f32 v2, v1, v6
	v_pk_fma_f32 v[4:5], v[44:45], v[14:15], v[4:5] op_sel_hi:[0,1,1] neg_lo:[0,0,1] neg_hi:[0,0,1]
	v_fma_mixhi_f16 v0, v44, v13, -v7 op_sel_hi:[0,0,1]
	v_cvt_pk_f16_f32 v1, v4, v5
	global_store_dwordx2 v[48:49], v[2:3], off offset:112
	global_store_dwordx2 v[18:19], v[0:1], off offset:112
	s_endpgm
	.p2alignl 8, 3212836864

	.amdhsa_kernel _Z9attn_mfmaPKDF16_S0_S0_S0_S0_S0_PDF16_S1_
		.amdhsa_group_segment_fixed_size 73728
		.amdhsa_private_segment_fixed_size 0
		.amdhsa_kernarg_size 64
		.amdhsa_user_sgpr_count 2
		.amdhsa_user_sgpr_dispatch_ptr 0
		.amdhsa_user_sgpr_queue_ptr 0
		.amdhsa_user_sgpr_kernarg_segment_ptr 1
		.amdhsa_user_sgpr_dispatch_id 0
		.amdhsa_user_sgpr_kernarg_preload_length 0
		.amdhsa_user_sgpr_kernarg_preload_offset 0
		.amdhsa_user_sgpr_private_segment_size 0
		.amdhsa_uses_dynamic_stack 0
		.amdhsa_enable_private_segment 0
		.amdhsa_system_sgpr_workgroup_id_x 1
		.amdhsa_system_sgpr_workgroup_id_y 1
		.amdhsa_system_sgpr_workgroup_id_z 0
		.amdhsa_system_sgpr_workgroup_info 0
		.amdhsa_system_vgpr_workitem_id 0
		.amdhsa_next_free_vgpr 252
		.amdhsa_next_free_sgpr 96
		.amdhsa_accum_offset 252
		.amdhsa_reserve_vcc 1
		.amdhsa_float_round_mode_32 0
		.amdhsa_float_round_mode_16_64 0
		.amdhsa_float_denorm_mode_32 3
		.amdhsa_float_denorm_mode_16_64 3
		.amdhsa_dx10_clamp 1
		.amdhsa_ieee_mode 1
		.amdhsa_fp16_overflow 0
		.amdhsa_tg_split 0
		.amdhsa_exception_fp_ieee_invalid_op 0
		.amdhsa_exception_fp_denorm_src 0
		.amdhsa_exception_fp_ieee_div_zero 0
		.amdhsa_exception_fp_ieee_overflow 0
		.amdhsa_exception_fp_ieee_underflow 0
		.amdhsa_exception_fp_ieee_inexact 0
		.amdhsa_exception_int_div_zero 0
	.end_amdhsa_kernel
